# P0 router-constant loop keeps 4 iterations of loads in flight and runs on the lightest workgroup; wg3 build and small weight conversions spread over more workgroups
# speedup vs baseline: 1.0094x; 1.0027x over previous
.LBB0_72:
	s_mov_b64 s[4:5], 0x1000
	global_load_dwordx4 v[12:15], v[4:5], off
	global_load_dwordx4 v[20:23], v[6:7], off
	global_load_dwordx4 v[16:19], v[4:5], off offset:16
	global_load_dwordx4 v[24:27], v[6:7], off offset:16
	global_load_dword v28, v[8:9], off offset:-896
	global_load_dword v29, v[8:9], off offset:-768
	global_load_dword v30, v[8:9], off offset:-640
	global_load_dword v31, v[8:9], off offset:-512
	global_load_dword v32, v[8:9], off offset:-384
	global_load_dword v33, v[8:9], off offset:-256
	global_load_dword v34, v[8:9], off offset:-128
	global_load_dword v35, v[8:9], off
	global_load_dwordx4 v[188:191], v[4:5], off offset:32
	global_load_dwordx4 v[196:199], v[6:7], off offset:32
	global_load_dwordx4 v[192:195], v[4:5], off offset:48
	global_load_dwordx4 v[200:203], v[6:7], off offset:48
	global_load_dword v204, v[8:9], off offset:128
	global_load_dword v205, v[8:9], off offset:256
	global_load_dword v206, v[8:9], off offset:384
	global_load_dword v207, v[8:9], off offset:512
	global_load_dword v208, v[8:9], off offset:640
	global_load_dword v209, v[8:9], off offset:768
	global_load_dword v210, v[8:9], off offset:896
	global_load_dword v211, v[8:9], off offset:1024
	global_load_dwordx4 v[212:215], v[4:5], off offset:64
	global_load_dwordx4 v[220:223], v[6:7], off offset:64
	global_load_dwordx4 v[216:219], v[4:5], off offset:80
	global_load_dwordx4 v[224:227], v[6:7], off offset:80
	global_load_dword v228, v[8:9], off offset:1152
	global_load_dword v229, v[8:9], off offset:1280
	global_load_dword v230, v[8:9], off offset:1408
	global_load_dword v231, v[8:9], off offset:1536
	global_load_dword v232, v[8:9], off offset:1664
	global_load_dword v233, v[8:9], off offset:1792
	global_load_dword v234, v[8:9], off offset:1920
	global_load_dword v235, v[8:9], off offset:2048
	global_load_dwordx4 v[236:239], v[4:5], off offset:96
	global_load_dwordx4 v[244:247], v[6:7], off offset:96
	global_load_dwordx4 v[240:243], v[4:5], off offset:112
	global_load_dwordx4 v[248:251], v[6:7], off offset:112
	global_load_dword v36, v[8:9], off offset:2176
	global_load_dword v37, v[8:9], off offset:2304
	global_load_dword v38, v[8:9], off offset:2432
	global_load_dword v39, v[8:9], off offset:2560
	global_load_dword v40, v[8:9], off offset:2688
	global_load_dword v41, v[8:9], off offset:2816
	global_load_dword v42, v[8:9], off offset:2944
	global_load_dword v43, v[8:9], off offset:3072
	v_lshl_add_u64 v[8:9], v[8:9], 0, s[4:5]
	s_waitcnt vmcnt(36)
	v_fmac_f32_e32 v2, v28, v12
	v_fmac_f32_e32 v3, v28, v20
	v_fmac_f32_e32 v2, v29, v13
	v_fmac_f32_e32 v3, v29, v21
	v_fmac_f32_e32 v2, v30, v14
	v_fmac_f32_e32 v3, v30, v22
	v_fmac_f32_e32 v2, v31, v15
	v_fmac_f32_e32 v3, v31, v23
	v_fmac_f32_e32 v2, v32, v16
	v_fmac_f32_e32 v3, v32, v24
	v_fmac_f32_e32 v2, v33, v17
	v_fmac_f32_e32 v3, v33, v25
	v_fmac_f32_e32 v2, v34, v18
	v_fmac_f32_e32 v3, v34, v26
	v_fmac_f32_e32 v2, v35, v19
	v_fmac_f32_e32 v3, v35, v27
	global_load_dwordx4 v[12:15], v[4:5], off offset:128
	global_load_dwordx4 v[20:23], v[6:7], off offset:128
	global_load_dwordx4 v[16:19], v[4:5], off offset:144
	global_load_dwordx4 v[24:27], v[6:7], off offset:144
	global_load_dword v28, v[8:9], off offset:-896
	global_load_dword v29, v[8:9], off offset:-768
	global_load_dword v30, v[8:9], off offset:-640
	global_load_dword v31, v[8:9], off offset:-512
	global_load_dword v32, v[8:9], off offset:-384
	global_load_dword v33, v[8:9], off offset:-256
	global_load_dword v34, v[8:9], off offset:-128
	global_load_dword v35, v[8:9], off
	s_waitcnt vmcnt(36)
	v_fmac_f32_e32 v2, v204, v188
	v_fmac_f32_e32 v3, v204, v196
	v_fmac_f32_e32 v2, v205, v189
	v_fmac_f32_e32 v3, v205, v197
	v_fmac_f32_e32 v2, v206, v190
	v_fmac_f32_e32 v3, v206, v198
	v_fmac_f32_e32 v2, v207, v191
	v_fmac_f32_e32 v3, v207, v199
	v_fmac_f32_e32 v2, v208, v192
	v_fmac_f32_e32 v3, v208, v200
	v_fmac_f32_e32 v2, v209, v193
	v_fmac_f32_e32 v3, v209, v201
	v_fmac_f32_e32 v2, v210, v194
	v_fmac_f32_e32 v3, v210, v202
	v_fmac_f32_e32 v2, v211, v195
	v_fmac_f32_e32 v3, v211, v203
	global_load_dwordx4 v[188:191], v[4:5], off offset:160
	global_load_dwordx4 v[196:199], v[6:7], off offset:160
	global_load_dwordx4 v[192:195], v[4:5], off offset:176
	global_load_dwordx4 v[200:203], v[6:7], off offset:176
	global_load_dword v204, v[8:9], off offset:128
	global_load_dword v205, v[8:9], off offset:256
	global_load_dword v206, v[8:9], off offset:384
	global_load_dword v207, v[8:9], off offset:512
	global_load_dword v208, v[8:9], off offset:640
	global_load_dword v209, v[8:9], off offset:768
	global_load_dword v210, v[8:9], off offset:896
	global_load_dword v211, v[8:9], off offset:1024
	s_waitcnt vmcnt(36)
	v_fmac_f32_e32 v2, v228, v212
	v_fmac_f32_e32 v3, v228, v220
	v_fmac_f32_e32 v2, v229, v213
	v_fmac_f32_e32 v3, v229, v221
	v_fmac_f32_e32 v2, v230, v214
	v_fmac_f32_e32 v3, v230, v222
	v_fmac_f32_e32 v2, v231, v215
	v_fmac_f32_e32 v3, v231, v223
	v_fmac_f32_e32 v2, v232, v216
	v_fmac_f32_e32 v3, v232, v224
	v_fmac_f32_e32 v2, v233, v217
	v_fmac_f32_e32 v3, v233, v225
	v_fmac_f32_e32 v2, v234, v218
	v_fmac_f32_e32 v3, v234, v226
	v_fmac_f32_e32 v2, v235, v219
	v_fmac_f32_e32 v3, v235, v227
	global_load_dwordx4 v[212:215], v[4:5], off offset:192
	global_load_dwordx4 v[220:223], v[6:7], off offset:192
	global_load_dwordx4 v[216:219], v[4:5], off offset:208
	global_load_dwordx4 v[224:227], v[6:7], off offset:208
	global_load_dword v228, v[8:9], off offset:1152
	global_load_dword v229, v[8:9], off offset:1280
	global_load_dword v230, v[8:9], off offset:1408
	global_load_dword v231, v[8:9], off offset:1536
	global_load_dword v232, v[8:9], off offset:1664
	global_load_dword v233, v[8:9], off offset:1792
	global_load_dword v234, v[8:9], off offset:1920
	global_load_dword v235, v[8:9], off offset:2048
	s_waitcnt vmcnt(36)
	v_fmac_f32_e32 v2, v36, v236
	v_fmac_f32_e32 v3, v36, v244
	v_fmac_f32_e32 v2, v37, v237
	v_fmac_f32_e32 v3, v37, v245
	v_fmac_f32_e32 v2, v38, v238
	v_fmac_f32_e32 v3, v38, v246
	v_fmac_f32_e32 v2, v39, v239
	v_fmac_f32_e32 v3, v39, v247
	v_fmac_f32_e32 v2, v40, v240
	v_fmac_f32_e32 v3, v40, v248
	v_fmac_f32_e32 v2, v41, v241
	v_fmac_f32_e32 v3, v41, v249
	v_fmac_f32_e32 v2, v42, v242
	v_fmac_f32_e32 v3, v42, v250
	v_fmac_f32_e32 v2, v43, v243
	v_fmac_f32_e32 v3, v43, v251
	global_load_dwordx4 v[236:239], v[4:5], off offset:224
	global_load_dwordx4 v[244:247], v[6:7], off offset:224
	global_load_dwordx4 v[240:243], v[4:5], off offset:240
	global_load_dwordx4 v[248:251], v[6:7], off offset:240
	global_load_dword v36, v[8:9], off offset:2176
	global_load_dword v37, v[8:9], off offset:2304
	global_load_dword v38, v[8:9], off offset:2432
	global_load_dword v39, v[8:9], off offset:2560
	global_load_dword v40, v[8:9], off offset:2688
	global_load_dword v41, v[8:9], off offset:2816
	global_load_dword v42, v[8:9], off offset:2944
	global_load_dword v43, v[8:9], off offset:3072
	v_lshl_add_u64 v[8:9], v[8:9], 0, s[4:5]
	s_waitcnt vmcnt(36)
	v_fmac_f32_e32 v2, v28, v12
	v_fmac_f32_e32 v3, v28, v20
	v_fmac_f32_e32 v2, v29, v13
	v_fmac_f32_e32 v3, v29, v21
	v_fmac_f32_e32 v2, v30, v14
	v_fmac_f32_e32 v3, v30, v22
	v_fmac_f32_e32 v2, v31, v15
	v_fmac_f32_e32 v3, v31, v23
	v_fmac_f32_e32 v2, v32, v16
	v_fmac_f32_e32 v3, v32, v24
	v_fmac_f32_e32 v2, v33, v17
	v_fmac_f32_e32 v3, v33, v25
	v_fmac_f32_e32 v2, v34, v18
	v_fmac_f32_e32 v3, v34, v26
	v_fmac_f32_e32 v2, v35, v19
	v_fmac_f32_e32 v3, v35, v27
	global_load_dwordx4 v[12:15], v[4:5], off offset:256
	global_load_dwordx4 v[20:23], v[6:7], off offset:256
	global_load_dwordx4 v[16:19], v[4:5], off offset:272
	global_load_dwordx4 v[24:27], v[6:7], off offset:272
	global_load_dword v28, v[8:9], off offset:-896
	global_load_dword v29, v[8:9], off offset:-768
	global_load_dword v30, v[8:9], off offset:-640
	global_load_dword v31, v[8:9], off offset:-512
	global_load_dword v32, v[8:9], off offset:-384
	global_load_dword v33, v[8:9], off offset:-256
	global_load_dword v34, v[8:9], off offset:-128
	global_load_dword v35, v[8:9], off
	s_waitcnt vmcnt(36)
	v_fmac_f32_e32 v2, v204, v188
	v_fmac_f32_e32 v3, v204, v196
	v_fmac_f32_e32 v2, v205, v189
	v_fmac_f32_e32 v3, v205, v197
	v_fmac_f32_e32 v2, v206, v190
	v_fmac_f32_e32 v3, v206, v198
	v_fmac_f32_e32 v2, v207, v191
	v_fmac_f32_e32 v3, v207, v199
	v_fmac_f32_e32 v2, v208, v192
	v_fmac_f32_e32 v3, v208, v200
	v_fmac_f32_e32 v2, v209, v193
	v_fmac_f32_e32 v3, v209, v201
	v_fmac_f32_e32 v2, v210, v194
	v_fmac_f32_e32 v3, v210, v202
	v_fmac_f32_e32 v2, v211, v195
	v_fmac_f32_e32 v3, v211, v203
	global_load_dwordx4 v[188:191], v[4:5], off offset:288
	global_load_dwordx4 v[196:199], v[6:7], off offset:288
	global_load_dwordx4 v[192:195], v[4:5], off offset:304
	global_load_dwordx4 v[200:203], v[6:7], off offset:304
	global_load_dword v204, v[8:9], off offset:128
	global_load_dword v205, v[8:9], off offset:256
	global_load_dword v206, v[8:9], off offset:384
	global_load_dword v207, v[8:9], off offset:512
	global_load_dword v208, v[8:9], off offset:640
	global_load_dword v209, v[8:9], off offset:768
	global_load_dword v210, v[8:9], off offset:896
	global_load_dword v211, v[8:9], off offset:1024
	s_waitcnt vmcnt(36)
	v_fmac_f32_e32 v2, v228, v212
	v_fmac_f32_e32 v3, v228, v220
	v_fmac_f32_e32 v2, v229, v213
	v_fmac_f32_e32 v3, v229, v221
	v_fmac_f32_e32 v2, v230, v214
	v_fmac_f32_e32 v3, v230, v222
	v_fmac_f32_e32 v2, v231, v215
	v_fmac_f32_e32 v3, v231, v223
	v_fmac_f32_e32 v2, v232, v216
	v_fmac_f32_e32 v3, v232, v224
	v_fmac_f32_e32 v2, v233, v217
	v_fmac_f32_e32 v3, v233, v225
	v_fmac_f32_e32 v2, v234, v218
	v_fmac_f32_e32 v3, v234, v226
	v_fmac_f32_e32 v2, v235, v219
	v_fmac_f32_e32 v3, v235, v227
	global_load_dwordx4 v[212:215], v[4:5], off offset:320
	global_load_dwordx4 v[220:223], v[6:7], off offset:320
	global_load_dwordx4 v[216:219], v[4:5], off offset:336
	global_load_dwordx4 v[224:227], v[6:7], off offset:336
	global_load_dword v228, v[8:9], off offset:1152
	global_load_dword v229, v[8:9], off offset:1280
	global_load_dword v230, v[8:9], off offset:1408
	global_load_dword v231, v[8:9], off offset:1536
	global_load_dword v232, v[8:9], off offset:1664
	global_load_dword v233, v[8:9], off offset:1792
	global_load_dword v234, v[8:9], off offset:1920
	global_load_dword v235, v[8:9], off offset:2048
	s_waitcnt vmcnt(36)
	v_fmac_f32_e32 v2, v36, v236
	v_fmac_f32_e32 v3, v36, v244
	v_fmac_f32_e32 v2, v37, v237
	v_fmac_f32_e32 v3, v37, v245
	v_fmac_f32_e32 v2, v38, v238
	v_fmac_f32_e32 v3, v38, v246
	v_fmac_f32_e32 v2, v39, v239
	v_fmac_f32_e32 v3, v39, v247
	v_fmac_f32_e32 v2, v40, v240
	v_fmac_f32_e32 v3, v40, v248
	v_fmac_f32_e32 v2, v41, v241
	v_fmac_f32_e32 v3, v41, v249
	v_fmac_f32_e32 v2, v42, v242
	v_fmac_f32_e32 v3, v42, v250
	v_fmac_f32_e32 v2, v43, v243
	v_fmac_f32_e32 v3, v43, v251
	global_load_dwordx4 v[236:239], v[4:5], off offset:352
	global_load_dwordx4 v[244:247], v[6:7], off offset:352
	global_load_dwordx4 v[240:243], v[4:5], off offset:368
	global_load_dwordx4 v[248:251], v[6:7], off offset:368
	global_load_dword v36, v[8:9], off offset:2176
	global_load_dword v37, v[8:9], off offset:2304
	global_load_dword v38, v[8:9], off offset:2432
	global_load_dword v39, v[8:9], off offset:2560
	global_load_dword v40, v[8:9], off offset:2688
	global_load_dword v41, v[8:9], off offset:2816
	global_load_dword v42, v[8:9], off offset:2944
	global_load_dword v43, v[8:9], off offset:3072
	v_lshl_add_u64 v[8:9], v[8:9], 0, s[4:5]
	s_waitcnt vmcnt(36)
	v_fmac_f32_e32 v2, v28, v12
	v_fmac_f32_e32 v3, v28, v20
	v_fmac_f32_e32 v2, v29, v13
	v_fmac_f32_e32 v3, v29, v21
	v_fmac_f32_e32 v2, v30, v14
	v_fmac_f32_e32 v3, v30, v22
	v_fmac_f32_e32 v2, v31, v15
	v_fmac_f32_e32 v3, v31, v23
	v_fmac_f32_e32 v2, v32, v16
	v_fmac_f32_e32 v3, v32, v24
	v_fmac_f32_e32 v2, v33, v17
	v_fmac_f32_e32 v3, v33, v25
	v_fmac_f32_e32 v2, v34, v18
	v_fmac_f32_e32 v3, v34, v26
	v_fmac_f32_e32 v2, v35, v19
	v_fmac_f32_e32 v3, v35, v27
	global_load_dwordx4 v[12:15], v[4:5], off offset:384
	global_load_dwordx4 v[20:23], v[6:7], off offset:384
	global_load_dwordx4 v[16:19], v[4:5], off offset:400
	global_load_dwordx4 v[24:27], v[6:7], off offset:400
	global_load_dword v28, v[8:9], off offset:-896
	global_load_dword v29, v[8:9], off offset:-768
	global_load_dword v30, v[8:9], off offset:-640
	global_load_dword v31, v[8:9], off offset:-512
	global_load_dword v32, v[8:9], off offset:-384
	global_load_dword v33, v[8:9], off offset:-256
	global_load_dword v34, v[8:9], off offset:-128
	global_load_dword v35, v[8:9], off
	s_waitcnt vmcnt(36)
	v_fmac_f32_e32 v2, v204, v188
	v_fmac_f32_e32 v3, v204, v196
	v_fmac_f32_e32 v2, v205, v189
	v_fmac_f32_e32 v3, v205, v197
	v_fmac_f32_e32 v2, v206, v190
	v_fmac_f32_e32 v3, v206, v198
	v_fmac_f32_e32 v2, v207, v191
	v_fmac_f32_e32 v3, v207, v199
	v_fmac_f32_e32 v2, v208, v192
	v_fmac_f32_e32 v3, v208, v200
	v_fmac_f32_e32 v2, v209, v193
	v_fmac_f32_e32 v3, v209, v201
	v_fmac_f32_e32 v2, v210, v194
	v_fmac_f32_e32 v3, v210, v202
	v_fmac_f32_e32 v2, v211, v195
	v_fmac_f32_e32 v3, v211, v203
	global_load_dwordx4 v[188:191], v[4:5], off offset:416
	global_load_dwordx4 v[196:199], v[6:7], off offset:416
	global_load_dwordx4 v[192:195], v[4:5], off offset:432
	global_load_dwordx4 v[200:203], v[6:7], off offset:432
	global_load_dword v204, v[8:9], off offset:128
	global_load_dword v205, v[8:9], off offset:256
	global_load_dword v206, v[8:9], off offset:384
	global_load_dword v207, v[8:9], off offset:512
	global_load_dword v208, v[8:9], off offset:640
	global_load_dword v209, v[8:9], off offset:768
	global_load_dword v210, v[8:9], off offset:896
	global_load_dword v211, v[8:9], off offset:1024
	s_waitcnt vmcnt(36)
	v_fmac_f32_e32 v2, v228, v212
	v_fmac_f32_e32 v3, v228, v220
	v_fmac_f32_e32 v2, v229, v213
	v_fmac_f32_e32 v3, v229, v221
	v_fmac_f32_e32 v2, v230, v214
	v_fmac_f32_e32 v3, v230, v222
	v_fmac_f32_e32 v2, v231, v215
	v_fmac_f32_e32 v3, v231, v223
	v_fmac_f32_e32 v2, v232, v216
	v_fmac_f32_e32 v3, v232, v224
	v_fmac_f32_e32 v2, v233, v217
	v_fmac_f32_e32 v3, v233, v225
	v_fmac_f32_e32 v2, v234, v218
	v_fmac_f32_e32 v3, v234, v226
	v_fmac_f32_e32 v2, v235, v219
	v_fmac_f32_e32 v3, v235, v227
	global_load_dwordx4 v[212:215], v[4:5], off offset:448
	global_load_dwordx4 v[220:223], v[6:7], off offset:448
	global_load_dwordx4 v[216:219], v[4:5], off offset:464
	global_load_dwordx4 v[224:227], v[6:7], off offset:464
	global_load_dword v228, v[8:9], off offset:1152
	global_load_dword v229, v[8:9], off offset:1280
	global_load_dword v230, v[8:9], off offset:1408
	global_load_dword v231, v[8:9], off offset:1536
	global_load_dword v232, v[8:9], off offset:1664
	global_load_dword v233, v[8:9], off offset:1792
	global_load_dword v234, v[8:9], off offset:1920
	global_load_dword v235, v[8:9], off offset:2048
	s_waitcnt vmcnt(36)
	v_fmac_f32_e32 v2, v36, v236
	v_fmac_f32_e32 v3, v36, v244
	v_fmac_f32_e32 v2, v37, v237
	v_fmac_f32_e32 v3, v37, v245
	v_fmac_f32_e32 v2, v38, v238
	v_fmac_f32_e32 v3, v38, v246
	v_fmac_f32_e32 v2, v39, v239
	v_fmac_f32_e32 v3, v39, v247
	v_fmac_f32_e32 v2, v40, v240
	v_fmac_f32_e32 v3, v40, v248
	v_fmac_f32_e32 v2, v41, v241
	v_fmac_f32_e32 v3, v41, v249
	v_fmac_f32_e32 v2, v42, v242
	v_fmac_f32_e32 v3, v42, v250
	v_fmac_f32_e32 v2, v43, v243
	v_fmac_f32_e32 v3, v43, v251
	global_load_dwordx4 v[236:239], v[4:5], off offset:480
	global_load_dwordx4 v[244:247], v[6:7], off offset:480
	global_load_dwordx4 v[240:243], v[4:5], off offset:496
	global_load_dwordx4 v[248:251], v[6:7], off offset:496
	global_load_dword v36, v[8:9], off offset:2176
	global_load_dword v37, v[8:9], off offset:2304
	global_load_dword v38, v[8:9], off offset:2432
	global_load_dword v39, v[8:9], off offset:2560
	global_load_dword v40, v[8:9], off offset:2688
	global_load_dword v41, v[8:9], off offset:2816
	global_load_dword v42, v[8:9], off offset:2944
	global_load_dword v43, v[8:9], off offset:3072
	v_lshl_add_u64 v[8:9], v[8:9], 0, s[4:5]
	s_waitcnt vmcnt(36)
	v_fmac_f32_e32 v2, v28, v12
	v_fmac_f32_e32 v3, v28, v20
	v_fmac_f32_e32 v2, v29, v13
	v_fmac_f32_e32 v3, v29, v21
	v_fmac_f32_e32 v2, v30, v14
	v_fmac_f32_e32 v3, v30, v22
	v_fmac_f32_e32 v2, v31, v15
	v_fmac_f32_e32 v3, v31, v23
	v_fmac_f32_e32 v2, v32, v16
	v_fmac_f32_e32 v3, v32, v24
	v_fmac_f32_e32 v2, v33, v17
	v_fmac_f32_e32 v3, v33, v25
	v_fmac_f32_e32 v2, v34, v18
	v_fmac_f32_e32 v3, v34, v26
	v_fmac_f32_e32 v2, v35, v19
	v_fmac_f32_e32 v3, v35, v27
	s_waitcnt vmcnt(24)
	v_fmac_f32_e32 v2, v204, v188
	v_fmac_f32_e32 v3, v204, v196
	v_fmac_f32_e32 v2, v205, v189
	v_fmac_f32_e32 v3, v205, v197
	v_fmac_f32_e32 v2, v206, v190
	v_fmac_f32_e32 v3, v206, v198
	v_fmac_f32_e32 v2, v207, v191
	v_fmac_f32_e32 v3, v207, v199
	v_fmac_f32_e32 v2, v208, v192
	v_fmac_f32_e32 v3, v208, v200
	v_fmac_f32_e32 v2, v209, v193
	v_fmac_f32_e32 v3, v209, v201
	v_fmac_f32_e32 v2, v210, v194
	v_fmac_f32_e32 v3, v210, v202
	v_fmac_f32_e32 v2, v211, v195
	v_fmac_f32_e32 v3, v211, v203
	s_waitcnt vmcnt(12)
	v_fmac_f32_e32 v2, v228, v212
	v_fmac_f32_e32 v3, v228, v220
	v_fmac_f32_e32 v2, v229, v213
	v_fmac_f32_e32 v3, v229, v221
	v_fmac_f32_e32 v2, v230, v214
	v_fmac_f32_e32 v3, v230, v222
	v_fmac_f32_e32 v2, v231, v215
	v_fmac_f32_e32 v3, v231, v223
	v_fmac_f32_e32 v2, v232, v216
	v_fmac_f32_e32 v3, v232, v224
	v_fmac_f32_e32 v2, v233, v217
	v_fmac_f32_e32 v3, v233, v225
	v_fmac_f32_e32 v2, v234, v218
	v_fmac_f32_e32 v3, v234, v226
	v_fmac_f32_e32 v2, v235, v219
	v_fmac_f32_e32 v3, v235, v227
	s_waitcnt vmcnt(0)
	v_fmac_f32_e32 v2, v36, v236
	v_fmac_f32_e32 v3, v36, v244
	v_fmac_f32_e32 v2, v37, v237
	v_fmac_f32_e32 v3, v37, v245
	v_fmac_f32_e32 v2, v38, v238
	v_fmac_f32_e32 v3, v38, v246
	v_fmac_f32_e32 v2, v39, v239
	v_fmac_f32_e32 v3, v39, v247
	v_fmac_f32_e32 v2, v40, v240
	v_fmac_f32_e32 v3, v40, v248
	v_fmac_f32_e32 v2, v41, v241
	v_fmac_f32_e32 v3, v41, v249
	v_fmac_f32_e32 v2, v42, v242
	v_fmac_f32_e32 v3, v42, v250
	v_fmac_f32_e32 v2, v43, v243
	v_fmac_f32_e32 v3, v43, v251
	s_add_i32 s0, 0, 0x10000
	v_and_b32_e32 v5, 0x1e0, v0
	v_lshl_add_u32 v4, v0, 2, s0
	ds_write_b32 v4, v2
	v_lshlrev_b32_e32 v2, 2, v5
	v_add3_u32 v2, s0, v2, v10
	v_cmp_gt_u32_e32 vcc, 32, v0
	ds_write_b32 v2, v3 offset:2048
	s_waitcnt lgkmcnt(0)
	s_barrier
	s_and_saveexec_b64 s[0:1], vcc
	s_cbranch_execz .LBB0_75
	v_lshlrev_b32_e32 v2, 2, v0
	global_load_dword v38, v2, s[60:61]
	ds_read2_b32 v[6:7], v4 offset1:32
	v_add_u32_e32 v18, 0x800, v4
	ds_read2_b32 v[8:9], v4 offset0:64 offset1:96
	ds_read2_b32 v[10:11], v4 offset0:128 offset1:160
	ds_read2_b32 v[12:13], v4 offset0:192 offset1:224
	v_add_u32_e32 v32, 0x400, v4
	v_add_u32_e32 v34, 0xc00, v4
	ds_read2_b32 v[4:5], v18 offset1:32
	ds_read2_b32 v[14:15], v18 offset0:64 offset1:96
	ds_read2_b32 v[16:17], v18 offset0:128 offset1:160
	ds_read2_b32 v[18:19], v18 offset0:192 offset1:224
	ds_read2_b32 v[20:21], v32 offset1:32
	ds_read2_b32 v[22:23], v34 offset1:32
	ds_read2_b32 v[24:25], v32 offset0:64 offset1:96
	ds_read2_b32 v[26:27], v34 offset0:64 offset1:96
	ds_read2_b32 v[28:29], v32 offset0:128 offset1:160
	ds_read2_b32 v[30:31], v34 offset0:128 offset1:160
	ds_read2_b32 v[32:33], v32 offset0:192 offset1:224
	ds_read2_b32 v[34:35], v34 offset0:192 offset1:224
	s_waitcnt lgkmcnt(14)
	v_add_f32_e32 v6, 0, v6
	v_add_f32_e32 v6, v6, v7
	v_add_f32_e32 v6, v6, v8
	v_add_f32_e32 v6, v6, v9
	s_waitcnt lgkmcnt(13)
	v_add_f32_e32 v6, v6, v10
	v_add_f32_e32 v6, v6, v11
	s_waitcnt lgkmcnt(12)
	v_add_f32_e32 v6, v6, v12
	v_add_f32_e32 v6, v6, v13
	s_waitcnt lgkmcnt(7)
	v_add_f32_e32 v6, v6, v20
	v_add_f32_e32 v6, v6, v21
	s_waitcnt lgkmcnt(5)
	v_add_f32_e32 v6, v6, v24
	v_add_f32_e32 v6, v6, v25
	v_mov_b32_e32 v3, 0
	s_waitcnt lgkmcnt(3)
	v_add_f32_e32 v6, v6, v28
	s_mov_b64 s[4:5], 0x180000
	v_lshl_add_u64 v[2:3], s[92:93], 0, v[2:3]
	v_add_f32_e32 v6, v6, v29
	v_lshl_add_u64 v[36:37], v[2:3], 0, s[4:5]
	v_add_co_u32_e32 v2, vcc, 0x180000, v2
	s_waitcnt lgkmcnt(1)
	v_add_f32_e32 v6, v6, v32
	v_addc_co_u32_e32 v3, vcc, 0, v3, vcc
	v_add_f32_e32 v6, v6, v33
	s_waitcnt vmcnt(0)
	v_add_f32_e32 v4, v38, v4
	v_add_f32_e32 v4, v4, v5
	v_add_f32_e32 v4, v4, v14
	v_add_f32_e32 v4, v4, v15
	v_add_f32_e32 v4, v4, v16
	v_add_f32_e32 v4, v4, v17
	v_add_f32_e32 v4, v4, v18
	v_add_f32_e32 v4, v4, v19
	v_add_f32_e32 v4, v4, v22
	v_add_f32_e32 v4, v4, v23
	v_add_f32_e32 v4, v4, v26
	v_add_f32_e32 v4, v4, v27
	v_add_f32_e32 v4, v4, v30
	v_add_f32_e32 v4, v4, v31
	s_waitcnt lgkmcnt(0)
	v_add_f32_e32 v4, v4, v34
	v_add_f32_e32 v4, v4, v35
	global_store_dword v[2:3], v6, off
	global_store_dword v[36:37], v4, off offset:128

.LBB0_76:
	s_sub_i32 s98, s96, 0xe0
	s_and_b32 s98, s98, 0xff
	v_lshl_or_b32 v2, s98, 9, v0
	s_movk_i32 s0, 0x2000
	v_cmp_gt_i32_e32 vcc, s0, v2
	s_and_saveexec_b64 s[0:1], vcc
	s_cbranch_execz .LBB0_79
	s_add_u32 s4, s92, 0x79500000
	s_addc_u32 s5, s93, 0
	s_lshl_b32 s6, s98, 12
	v_lshlrev_b32_e32 v3, 3, v0
	s_lshl_b32 s3, s90, 9
	v_or3_b32 v3, s6, v3, 7
	s_lshl_b32 s8, s90, 12
	s_mov_b64 s[6:7], 0
	s_mov_b32 s9, 0x20000
	s_movk_i32 s10, 0x1fff

.LBB0_204:
	s_sub_i32 s7, s7, 0x200
	s_and_b32 s7, s7, 0x7ff
	s_cmpk_lt_i32 s7, 0x200
	s_cselect_b64 s[0:1], -1, 0
	v_mov_b32_e32 v50, v1
	s_andn2_b64 vcc, exec, s[0:1]
	s_cbranch_vccnz .LBB0_213
	v_readlane_b32 s56, v254, 13
	v_readlane_b32 s70, v254, 27
	v_readlane_b32 s71, v254, 28
	s_add_u32 s4, s70, 0x800000
	s_addc_u32 s5, s71, 0
	s_add_u32 s9, s92, 0xc00000
	s_addc_u32 s10, s93, 0
	s_ashr_i32 s0, s7, 31
	s_lshr_b32 s0, s0, 23
	s_add_i32 s0, s7, s0
	s_and_b32 s0, s0, 0xfffffe00
	s_sub_i32 s1, s7, s0
	s_bfe_u32 s0, s1, 0x60019
	s_add_i32 s0, s1, s0
	s_sext_i32_i16 s0, s0
	s_lshr_b32 s0, s0, 6
	s_bfe_i64 s[12:13], s[0:1], 0x100000
	s_lshl_b64 s[12:13], s[12:13], 20
	s_add_u32 s11, s4, s12
	s_addc_u32 s12, s5, s13
	s_lshl_b32 s0, s0, 11
	s_lshl_b32 s1, s1, 5
	s_sub_i32 s0, s1, s0
	s_ashr_i32 s1, s0, 31
	s_lshl_b64 s[0:1], s[0:1], 2
	s_waitcnt vmcnt(18)
	v_lshlrev_b32_e32 v3, 4, v50
	s_add_u32 s0, s11, s0
	v_lshlrev_b32_e32 v2, 12, v50
	v_and_b32_e32 v3, 0x70, v3
	s_movk_i32 s11, 0x8000
	s_addc_u32 s1, s12, s1
	v_and_or_b32 v130, v2, s11, v3
	v_mov_b32_e32 v131, 0
	v_lshl_add_u64 v[30:31], s[0:1], 0, v[130:131]
	s_movk_i32 s11, 0x2000
	v_add_co_u32_e32 v2, vcc, s11, v30
	s_movk_i32 s12, 0x4000
	s_nop 0
	v_addc_co_u32_e32 v3, vcc, 0, v31, vcc
	s_waitcnt vmcnt(17)
	v_add_co_u32_e32 v6, vcc, s12, v30
	s_movk_i32 s13, 0x6000
	s_nop 0
	v_addc_co_u32_e32 v7, vcc, 0, v31, vcc
	s_waitcnt vmcnt(16)
	v_add_co_u32_e32 v10, vcc, s13, v30
	s_mov_b32 s14, 0x40000
	s_nop 0
	v_addc_co_u32_e32 v11, vcc, 0, v31, vcc
	s_waitcnt vmcnt(15)
	v_add_co_u32_e32 v14, vcc, s14, v30
	s_mov_b32 s15, 0x42000
	s_nop 0
	v_addc_co_u32_e32 v15, vcc, 0, v31, vcc
	s_waitcnt vmcnt(14)
	v_add_co_u32_e32 v18, vcc, s15, v30
	s_mov_b32 s20, 0x44000
	s_nop 0
	v_addc_co_u32_e32 v19, vcc, 0, v31, vcc
	s_waitcnt vmcnt(13)
	v_add_co_u32_e32 v22, vcc, s20, v30
	s_mov_b32 s21, 0x46000
	s_nop 0
	v_addc_co_u32_e32 v23, vcc, 0, v31, vcc
	s_waitcnt vmcnt(12)
	v_add_co_u32_e32 v26, vcc, s21, v30
	s_mov_b32 s22, 0x80000
	s_nop 0
	v_addc_co_u32_e32 v27, vcc, 0, v31, vcc
	v_add_co_u32_e32 v32, vcc, s22, v30
	s_mov_b32 s23, 0x82000
	s_nop 0
	v_addc_co_u32_e32 v33, vcc, 0, v31, vcc
	global_load_dwordx4 v[2:5], v[2:3], off nt
	s_nop 0
	global_load_dwordx4 v[6:9], v[6:7], off nt
	s_nop 0
	global_load_dwordx4 v[10:13], v[10:11], off nt
	s_nop 0
	global_load_dwordx4 v[14:17], v[14:15], off nt
	s_nop 0
	global_load_dwordx4 v[18:21], v[18:19], off nt
	s_nop 0
	global_load_dwordx4 v[22:25], v[22:23], off nt
	s_nop 0
	global_load_dwordx4 v[26:29], v[26:27], off nt
	s_nop 0
	global_load_dwordx4 v[34:37], v[32:33], off nt
	v_add_co_u32_e32 v32, vcc, s23, v30
	s_mov_b32 s24, 0x84000
	s_nop 0
	v_addc_co_u32_e32 v33, vcc, 0, v31, vcc
	s_waitcnt vmcnt(17)
	v_add_co_u32_e32 v42, vcc, s24, v30
	s_mov_b32 s25, 0x86000
	s_nop 0
	v_addc_co_u32_e32 v43, vcc, 0, v31, vcc
	global_load_dwordx4 v[38:41], v[32:33], off nt
	s_nop 0
	global_load_dwordx4 v[42:45], v[42:43], off nt
	v_add_co_u32_e32 v32, vcc, s25, v30
	s_mov_b32 s26, 0xc0000
	s_nop 0
	v_addc_co_u32_e32 v33, vcc, 0, v31, vcc
	v_add_co_u32_e32 v52, vcc, s26, v30
	s_mov_b32 s27, 0xc2000
	s_nop 0
	v_addc_co_u32_e32 v53, vcc, 0, v31, vcc
	global_load_dwordx4 v[46:49], v[32:33], off nt
	global_load_dwordx4 v[58:61], v[52:53], off nt
	v_add_co_u32_e32 v32, vcc, s27, v30
	s_mov_b32 s27, 0xc4000
	s_nop 0
	v_addc_co_u32_e32 v33, vcc, 0, v31, vcc
	v_add_co_u32_e32 v52, vcc, s27, v30
	s_mov_b32 s27, 0xc6000
	s_nop 0
	v_addc_co_u32_e32 v53, vcc, 0, v31, vcc
	global_load_dwordx4 v[70:73], v[32:33], off nt
	global_load_dwordx4 v[82:85], v[52:53], off nt
	v_add_co_u32_e32 v52, vcc, s27, v30
	v_and_b32_e32 v51, 7, v50
	s_nop 0
	v_addc_co_u32_e32 v53, vcc, 0, v31, vcc
	global_load_dwordx4 v[30:33], v130, s[0:1] nt
	global_load_dwordx4 v[94:97], v[52:53], off nt
	v_ashrrev_i32_e32 v52, 3, v50
	v_lshlrev_b32_e32 v57, 4, v51
	v_lshlrev_b32_e32 v54, 2, v52
	v_lshl_or_b32 v132, v52, 10, v57
	v_lshl_add_u32 v57, v52, 7, s8
	v_lshrrev_b32_e32 v62, 1, v52
	v_add_u32_e32 v63, 8, v52
	v_add_u32_e32 v52, 24, v52
	v_lshl_add_u32 v64, v63, 7, s8
	v_lshrrev_b32_e32 v63, 1, v63
	v_lshl_add_u32 v65, v52, 7, s8
	v_lshrrev_b32_e32 v52, 1, v52
	v_lshlrev_b32_e32 v53, 9, v51
	v_lshlrev_b32_e32 v50, 5, v50
	s_movk_i32 s0, 0x60
	v_mov_b32_e32 v55, 0x60
	v_bitop3_b32 v62, v62, v51, 6 bitop3:0x6c
	v_bitop3_b32 v63, v63, v51, 6 bitop3:0x6c
	v_bitop3_b32 v51, v52, v51, 6 bitop3:0x6c
	v_add3_u32 v53, s8, v53, v54
	v_and_b32_e32 v54, 0x60, v50
	v_bitop3_b32 v56, v50, 32, v55 bitop3:0x6c
	v_bitop3_b32 v55, v50, 64, v55 bitop3:0x6c
	v_bitop3_b32 v50, v50, s0, v50 bitop3:0xc
	v_lshlrev_b32_e32 v62, 4, v62
	v_lshlrev_b32_e32 v63, 4, v63
	v_lshlrev_b32_e32 v51, 4, v51
	v_mov_b32_e32 v133, v131
	s_lshl_b32 s27, s90, 4
	v_add_u32_e32 v134, v53, v54
	v_add_u32_e32 v135, v53, v56
	v_add_u32_e32 v136, v53, v55
	v_add_u32_e32 v137, v53, v50
	v_add_u32_e32 v138, v57, v62
	v_add_u32_e32 v139, v64, v63
	v_add_u32_e32 v140, v65, v51
	s_mov_b32 s28, s7
	v_readlane_b32 s57, v254, 14
	v_readlane_b32 s58, v254, 15
	v_readlane_b32 s59, v254, 16
	v_readlane_b32 s60, v254, 17
	v_readlane_b32 s61, v254, 18
	v_readlane_b32 s62, v254, 19
	v_readlane_b32 s63, v254, 20
	v_readlane_b32 s64, v254, 21
	v_readlane_b32 s65, v254, 22
	v_readlane_b32 s66, v254, 23
	v_readlane_b32 s67, v254, 24
	v_readlane_b32 s68, v254, 25
	v_readlane_b32 s69, v254, 26
	s_branch .LBB0_208

.LBB0_213:
	s_sub_i32 s7, s7, 0x200
	s_and_b32 s7, s7, 0x7ff
	v_mov_b32_e32 v50, v1
	s_cmpk_gt_i32 s7, 0x3ff
	s_cbranch_scc1 .LBB0_222
	s_add_u32 s4, s92, 0x1000000
	s_addc_u32 s5, s93, 0
	s_ashr_i32 s0, s7, 31
	s_lshr_b32 s0, s0, 22
	s_add_i32 s0, s7, s0
	s_and_b32 s0, s0, 0xfffffc00
	s_sub_i32 s1, s7, s0
	s_bfe_u32 s0, s1, 0x60019
	s_add_i32 s0, s1, s0
	s_sext_i32_i16 s0, s0
	s_lshr_b32 s0, s0, 6
	s_bfe_i64 s[10:11], s[0:1], 0x100000
	s_lshl_b64 s[10:11], s[10:11], 20
	s_add_u32 s9, s52, s10
	s_addc_u32 s10, s53, s11
	s_lshl_b32 s0, s0, 11
	s_lshl_b32 s1, s1, 5
	s_sub_i32 s0, s1, s0
	s_ashr_i32 s1, s0, 31
	s_lshl_b64 s[0:1], s[0:1], 2
	s_waitcnt vmcnt(18)
	v_lshlrev_b32_e32 v3, 4, v50
	s_add_u32 s0, s9, s0
	v_lshlrev_b32_e32 v2, 12, v50
	v_and_b32_e32 v3, 0x70, v3
	s_movk_i32 s9, 0x8000
	s_addc_u32 s1, s10, s1
	v_and_or_b32 v130, v2, s9, v3
	v_mov_b32_e32 v131, 0
	v_lshl_add_u64 v[30:31], s[0:1], 0, v[130:131]
	s_movk_i32 s9, 0x2000
	v_add_co_u32_e32 v2, vcc, s9, v30
	s_movk_i32 s10, 0x4000
	s_nop 0
	v_addc_co_u32_e32 v3, vcc, 0, v31, vcc
	s_waitcnt vmcnt(17)
	v_add_co_u32_e32 v6, vcc, s10, v30
	s_movk_i32 s11, 0x6000
	s_nop 0
	v_addc_co_u32_e32 v7, vcc, 0, v31, vcc
	s_waitcnt vmcnt(16)
	v_add_co_u32_e32 v10, vcc, s11, v30
	s_mov_b32 s12, 0x40000
	s_nop 0
	v_addc_co_u32_e32 v11, vcc, 0, v31, vcc
	s_waitcnt vmcnt(15)
	v_add_co_u32_e32 v14, vcc, s12, v30
	s_mov_b32 s13, 0x42000
	s_nop 0
	v_addc_co_u32_e32 v15, vcc, 0, v31, vcc
	s_waitcnt vmcnt(14)
	v_add_co_u32_e32 v18, vcc, s13, v30
	s_mov_b32 s14, 0x44000
	s_nop 0
	v_addc_co_u32_e32 v19, vcc, 0, v31, vcc
	s_waitcnt vmcnt(13)
	v_add_co_u32_e32 v22, vcc, s14, v30
	s_mov_b32 s15, 0x46000
	s_nop 0
	v_addc_co_u32_e32 v23, vcc, 0, v31, vcc
	s_waitcnt vmcnt(12)
	v_add_co_u32_e32 v26, vcc, s15, v30
	s_mov_b32 s20, 0x80000
	s_nop 0
	v_addc_co_u32_e32 v27, vcc, 0, v31, vcc
	v_add_co_u32_e32 v32, vcc, s20, v30
	s_mov_b32 s21, 0x82000
	s_nop 0
	v_addc_co_u32_e32 v33, vcc, 0, v31, vcc
	global_load_dwordx4 v[2:5], v[2:3], off nt
	s_nop 0
	global_load_dwordx4 v[6:9], v[6:7], off nt
	s_nop 0
	global_load_dwordx4 v[10:13], v[10:11], off nt
	s_nop 0
	global_load_dwordx4 v[14:17], v[14:15], off nt
	s_nop 0
	global_load_dwordx4 v[18:21], v[18:19], off nt
	s_nop 0
	global_load_dwordx4 v[22:25], v[22:23], off nt
	s_nop 0
	global_load_dwordx4 v[26:29], v[26:27], off nt
	s_nop 0
	global_load_dwordx4 v[34:37], v[32:33], off nt
	v_add_co_u32_e32 v32, vcc, s21, v30
	s_mov_b32 s22, 0x84000
	s_nop 0
	v_addc_co_u32_e32 v33, vcc, 0, v31, vcc
	s_waitcnt vmcnt(17)
	v_add_co_u32_e32 v42, vcc, s22, v30
	s_mov_b32 s23, 0x86000
	s_nop 0
	v_addc_co_u32_e32 v43, vcc, 0, v31, vcc
	global_load_dwordx4 v[38:41], v[32:33], off nt
	s_nop 0
	global_load_dwordx4 v[42:45], v[42:43], off nt
	v_add_co_u32_e32 v32, vcc, s23, v30
	s_mov_b32 s24, 0xc0000
	s_nop 0
	v_addc_co_u32_e32 v33, vcc, 0, v31, vcc
	v_add_co_u32_e32 v52, vcc, s24, v30
	s_mov_b32 s25, 0xc2000
	s_nop 0
	v_addc_co_u32_e32 v53, vcc, 0, v31, vcc
	global_load_dwordx4 v[46:49], v[32:33], off nt
	global_load_dwordx4 v[58:61], v[52:53], off nt
	v_add_co_u32_e32 v32, vcc, s25, v30
	s_mov_b32 s25, 0xc4000
	s_nop 0
	v_addc_co_u32_e32 v33, vcc, 0, v31, vcc
	v_add_co_u32_e32 v52, vcc, s25, v30
	s_mov_b32 s25, 0xc6000
	s_nop 0
	v_addc_co_u32_e32 v53, vcc, 0, v31, vcc
	global_load_dwordx4 v[70:73], v[32:33], off nt
	global_load_dwordx4 v[82:85], v[52:53], off nt
	v_add_co_u32_e32 v52, vcc, s25, v30
	v_and_b32_e32 v51, 7, v50
	s_nop 0
	v_addc_co_u32_e32 v53, vcc, 0, v31, vcc
	global_load_dwordx4 v[30:33], v130, s[0:1] nt
	global_load_dwordx4 v[94:97], v[52:53], off nt
	v_ashrrev_i32_e32 v52, 3, v50
	v_lshlrev_b32_e32 v57, 4, v51
	v_lshlrev_b32_e32 v54, 2, v52
	v_lshl_or_b32 v132, v52, 11, v57
	v_lshl_add_u32 v57, v52, 7, s8
	v_lshrrev_b32_e32 v62, 1, v52
	v_add_u32_e32 v63, 8, v52
	v_add_u32_e32 v52, 24, v52
	v_lshl_add_u32 v64, v63, 7, s8
	v_lshrrev_b32_e32 v63, 1, v63
	v_lshl_add_u32 v65, v52, 7, s8
	v_lshrrev_b32_e32 v52, 1, v52
	v_lshlrev_b32_e32 v53, 9, v51
	v_lshlrev_b32_e32 v50, 5, v50
	s_movk_i32 s0, 0x60
	v_mov_b32_e32 v55, 0x60
	v_bitop3_b32 v62, v62, v51, 6 bitop3:0x6c
	v_bitop3_b32 v63, v63, v51, 6 bitop3:0x6c
	v_bitop3_b32 v51, v52, v51, 6 bitop3:0x6c
	v_add3_u32 v53, s8, v53, v54
	v_and_b32_e32 v54, 0x60, v50
	v_bitop3_b32 v56, v50, 32, v55 bitop3:0x6c
	v_bitop3_b32 v55, v50, 64, v55 bitop3:0x6c
	v_bitop3_b32 v50, v50, s0, v50 bitop3:0xc
	v_lshlrev_b32_e32 v62, 4, v62
	v_lshlrev_b32_e32 v63, 4, v63
	v_lshlrev_b32_e32 v51, 4, v51
	v_mov_b32_e32 v133, v131
	s_lshl_b32 s8, s90, 4
	v_add_u32_e32 v134, v53, v54
	v_add_u32_e32 v135, v53, v56
	v_add_u32_e32 v136, v53, v55
	v_add_u32_e32 v137, v53, v50
	v_add_u32_e32 v138, v57, v62
	v_add_u32_e32 v139, v64, v63
	v_add_u32_e32 v140, v65, v51
	s_branch .LBB0_217

	.amdhsa_kernel _Z10fwd_kernel4Args
		.amdhsa_group_segment_fixed_size 0
		.amdhsa_private_segment_fixed_size 0
		.amdhsa_kernarg_size 432
		.amdhsa_user_sgpr_count 2
		.amdhsa_user_sgpr_dispatch_ptr 0
		.amdhsa_user_sgpr_queue_ptr 0
		.amdhsa_user_sgpr_kernarg_segment_ptr 1
		.amdhsa_user_sgpr_dispatch_id 0
		.amdhsa_user_sgpr_kernarg_preload_length 0
		.amdhsa_user_sgpr_kernarg_preload_offset 0
		.amdhsa_user_sgpr_private_segment_size 0
		.amdhsa_uses_dynamic_stack 0
		.amdhsa_enable_private_segment 0
		.amdhsa_system_sgpr_workgroup_id_x 1
		.amdhsa_system_sgpr_workgroup_id_y 0
		.amdhsa_system_sgpr_workgroup_id_z 0
		.amdhsa_system_sgpr_workgroup_info 0
		.amdhsa_system_vgpr_workitem_id 0
		.amdhsa_next_free_vgpr 255
		.amdhsa_next_free_sgpr 102
		.amdhsa_accum_offset 256
		.amdhsa_reserve_vcc 1
		.amdhsa_float_round_mode_32 0
		.amdhsa_float_round_mode_16_64 0
		.amdhsa_float_denorm_mode_32 3
		.amdhsa_float_denorm_mode_16_64 3
		.amdhsa_dx10_clamp 1
		.amdhsa_ieee_mode 1
		.amdhsa_fp16_overflow 0
		.amdhsa_tg_split 0
		.amdhsa_exception_fp_ieee_invalid_op 0
		.amdhsa_exception_fp_denorm_src 0
		.amdhsa_exception_fp_ieee_div_zero 0
		.amdhsa_exception_fp_ieee_overflow 0
		.amdhsa_exception_fp_ieee_underflow 0
		.amdhsa_exception_fp_ieee_inexact 0
		.amdhsa_exception_int_div_zero 0
	.end_amdhsa_kernel

amdhsa.kernels:
  - .agpr_count:     0
    .args:
      - .offset:         0
        .size:           176
        .value_kind:     by_value
      - .offset:         176
        .size:           4
        .value_kind:     hidden_block_count_x
      - .offset:         180
        .size:           4
        .value_kind:     hidden_block_count_y
      - .offset:         184
        .size:           4
        .value_kind:     hidden_block_count_z
      - .offset:         188
        .size:           2
        .value_kind:     hidden_group_size_x
      - .offset:         190
        .size:           2
        .value_kind:     hidden_group_size_y
      - .offset:         192
        .size:           2
        .value_kind:     hidden_group_size_z
      - .offset:         194
        .size:           2
        .value_kind:     hidden_remainder_x
      - .offset:         196
        .size:           2
        .value_kind:     hidden_remainder_y
      - .offset:         198
        .size:           2
        .value_kind:     hidden_remainder_z
      - .offset:         216
        .size:           8
        .value_kind:     hidden_global_offset_x
      - .offset:         224
        .size:           8
        .value_kind:     hidden_global_offset_y
      - .offset:         232
        .size:           8
        .value_kind:     hidden_global_offset_z
      - .offset:         240
        .size:           2
        .value_kind:     hidden_grid_dims
      - .offset:         296
        .size:           4
        .value_kind:     hidden_dynamic_lds_size
    .group_segment_fixed_size: 0
    .kernarg_segment_align: 8
    .kernarg_segment_size: 432
    .language:       OpenCL C
    .language_version:
      - 2
      - 0
    .max_flat_workgroup_size: 512
    .name:           _Z10fwd_kernel4Args
    .private_segment_fixed_size: 0
    .sgpr_count:     108
    .sgpr_spill_count: 68
    .symbol:         _Z10fwd_kernel4Args.kd
    .uniform_work_group_size: 1
    .uses_dynamic_stack: false
    .vgpr_count:     255
    .vgpr_spill_count: 0
    .wavefront_size: 64
